# v15 + cache policy: the expert-weight copy stores in the router phases lose the nt hint (weights are consumed by the next phase)
# baseline (speedup 1.0000x reference)
; #define GAS __attribute__((address_space(1)))
; __device__ __forceinline__ unsigned pk2(float lo, float hi) { return f2bf(lo) | (f2bf(hi) << 16); }
; #define NTLD(P) (NT_STREAMS ? __builtin_nontemporal_load(P) : *(P))
;     (void)scr;
;     const int nblk = N / 32, kb = item / nblk, nb = item % nblk, a = lane & 7, q = lane >> 3, k0 = 64 * kb + 8 * q, n0 = 32 * nb + 4 * a;
;     const GAS f32x4* src = (const GAS f32x4*)(W + (size_t)k0 * N + n0);
;     f32x4 r[8];
; #pragma unroll
;     for (int i = 0; i < 8; ++i) r[i] = NTLD(src + (size_t)i * (N / 4));
; #pragma unroll
;     for (int j = 0; j < 4; ++j) { v4u o; o.x = pk2(r[0][j] * scale, r[1][j] * scale); o.y = pk2(r[2][j] * scale, r[3][j] * scale); o.z = pk2(r[4][j] * scale, r[5][j] * scale); o.w = pk2(r[6][j] * scale, r[7][j] * scale);
;         if (NT_STREAMS) __builtin_nontemporal_store(o, (GAS v4u*)(WT + (size_t)maprow(mode, n0 + j) * K + k0)); else *(GAS v4u*)(WT + (size_t)maprow(mode, n0 + j) * K + k0) = o; }
;     ...
;     for (int it = it0 + gw; it < it1; it += NGW) {
;         const int e = it / 384, r = it % 384; const size_t eo = (size_t)(layer * 64 + e) * 1024 * 256;
;         if (r < 128) p0_transpose_item(inp(F, I_WGATE) + eo, 1024, 256, UP + (size_t)e * 512 * 1024, 3, scr, r, F.lane);
;         else if (r < 256) p0_transpose_item(inp(F, I_WUP) + eo, 1024, 256, UP + (size_t)e * 512 * 1024, 4, scr, r - 128, F.lane);
;         else p0_transpose_item(inp(F, I_WDOWN) + eo, 256, 1024, DN + (size_t)e * 1024 * 256, 5, scr, r - 256, F.lane, 16.f);
.Lcv0_06:
	s_add_i32 s5, s5, s2
	s_add_i32 s21, s21, s22
	s_add_i32 s23, s23, s40
	s_add_i32 s41, s41, s42
	s_add_i32 s43, s43, s44
	s_cmpk_lt_i32 s5, 0x6000
	s_waitcnt lgkmcnt(0)
	global_store_dwordx4 v[8:9], v[2:5], off
	s_cbranch_scc0 .Lcv0_end
.Lcv0_07:
	s_mul_hi_i32 s12, s5, 0x2aaaaaab
	s_lshr_b32 s13, s12, 31
	s_ashr_i32 s12, s12, 6
	s_add_i32 s12, s12, s13
	s_mul_i32 s13, s12, 0xfffffe80
	s_add_i32 s54, s5, s13
	s_ashr_i32 s13, s12, 31
	s_lshl_b64 s[14:15], s[12:13], 18
	s_add_u32 s14, s14, 0
	s_addc_u32 s15, s15, 0
	s_cmpk_gt_i32 s54, 0x7f
	s_mov_b64 s[16:17], -1
	s_cbranch_scc0 .Lcv0_13
	s_cmpk_gt_u32 s54, 0xff
	s_cbranch_scc0 .Lcv0_10
	v_mov_b32_e32 v2, s45
	ds_read_b64 v[2:3], v2
	s_lshl_b64 s[16:17], s[14:15], 2
	s_waitcnt lgkmcnt(0)
	v_readfirstlane_b32 s30, v2
	v_readfirstlane_b32 s31, v3
	s_add_u32 s16, s30, s16
	s_addc_u32 s17, s31, s17
	s_lshl_b64 s[56:57], s[12:13], 19
	s_add_u32 s56, s19, s56
	s_addc_u32 s57, s20, s57
	s_lshl_b32 s30, s12, 8
	s_sub_i32 s30, s43, s30
	s_and_b32 s30, s30, 0x1c0
	v_or_b32_e32 v42, s30, v1
	s_and_b32 s30, s23, 0x3e0
	v_or_b32_e32 v4, s30, v10
	v_lshlrev_b32_e32 v6, 12, v42
	v_lshl_add_u64 v[2:3], s[16:17], 0, v[6:7]
	v_lshlrev_b32_e32 v6, 2, v4
	v_lshl_add_u64 v[8:9], v[2:3], 0, v[6:7]
	v_add_co_u32_e32 v18, vcc, s3, v8
	global_load_dwordx4 v[2:5], v[8:9], off nt
	s_nop 0
	v_addc_co_u32_e32 v19, vcc, 0, v9, vcc
	v_add_co_u32_e32 v26, vcc, s47, v8
	global_load_dwordx4 v[14:17], v[18:19], off offset:-4096 nt
	s_nop 0
	global_load_dwordx4 v[18:21], v[18:19], off nt
	v_addc_co_u32_e32 v27, vcc, 0, v9, vcc
	v_add_co_u32_e32 v34, vcc, s48, v8
	global_load_dwordx4 v[22:25], v[26:27], off offset:-4096 nt
	s_nop 0
	global_load_dwordx4 v[26:29], v[26:27], off nt
	v_addc_co_u32_e32 v35, vcc, 0, v9, vcc
	v_add_co_u32_e32 v8, vcc, s49, v8
	global_load_dwordx4 v[30:33], v[34:35], off offset:-4096 nt
	s_nop 0
	global_load_dwordx4 v[34:37], v[34:35], off nt
	v_addc_co_u32_e32 v9, vcc, 0, v9, vcc
	global_load_dwordx4 v[38:41], v[8:9], off nt
	s_lshr_b32 s16, s54, 1
	v_lshlrev_b32_e32 v8, 1, v42
	v_and_b32_e32 v6, 0x3f0, v6
	v_mov_b32_e32 v9, v7
	v_and_or_b32 v6, s16, 12, v6
	v_lshl_add_u64 v[8:9], s[56:57], 0, v[8:9]
	v_lshlrev_b32_e32 v6, 9, v6
	v_lshl_add_u64 v[8:9], v[8:9], 0, v[6:7]
	s_mov_b64 s[16:17], 0
	s_waitcnt vmcnt(7)
	v_mov_b32_e32 v42, v2
	s_waitcnt vmcnt(6)
	v_mov_b32_e32 v44, v14
	s_waitcnt vmcnt(5)
	v_mov_b32_e32 v43, v18
	v_mov_b32_e32 v18, v3
	v_pk_mul_f32 v[2:3], v[42:43], s[4:5] op_sel_hi:[1,0]
	v_pk_mul_f32 v[18:19], v[18:19], s[4:5] op_sel_hi:[1,0]
	s_waitcnt vmcnt(4)
	v_mov_b32_e32 v45, v22
	s_waitcnt vmcnt(3)
	v_mov_b32_e32 v46, v26
	v_mov_b32_e32 v22, v15
	v_pk_mul_f32 v[14:15], v[44:45], s[4:5] op_sel_hi:[1,0]
	v_pk_mul_f32 v[22:23], v[22:23], s[4:5] op_sel_hi:[1,0]
	s_waitcnt vmcnt(2)
	v_mov_b32_e32 v48, v30
	s_waitcnt vmcnt(1)
	v_mov_b32_e32 v47, v34
	v_mov_b32_e32 v34, v27
	v_pk_mul_f32 v[26:27], v[46:47], s[4:5] op_sel_hi:[1,0]
	s_waitcnt vmcnt(0)
	v_mov_b32_e32 v49, v38
	v_mov_b32_e32 v38, v31
	v_pk_mul_f32 v[30:31], v[48:49], s[4:5] op_sel_hi:[1,0]
	v_bfe_u32 v46, v27, 16, 1
	v_bfe_u32 v47, v2, 16, 1
	v_bfe_u32 v6, v31, 16, 1
	v_bfe_u32 v44, v14, 16, 1
	v_bfe_u32 v48, v3, 16, 1
	v_add3_u32 v27, v27, v46, s50
	v_add3_u32 v2, v2, v47, s50
	v_bfe_u32 v42, v30, 16, 1
	v_bfe_u32 v43, v15, 16, 1
	v_bfe_u32 v45, v26, 16, 1
	v_add3_u32 v14, v14, v44, s50
	v_add3_u32 v6, v31, v6, s50
	v_add3_u32 v3, v3, v48, s50
	v_lshrrev_b32_e32 v27, 16, v27
	v_lshrrev_b32_e32 v2, 16, v2
	v_pk_mul_f32 v[34:35], v[34:35], s[4:5] op_sel_hi:[1,0]
	v_add3_u32 v15, v15, v43, s50
	v_add3_u32 v30, v30, v42, s50
	v_add3_u32 v26, v26, v45, s50
	v_lshrrev_b32_e32 v3, 16, v3
	v_and_or_b32 v45, v6, s51, v27
	v_and_or_b32 v42, v14, s51, v2
	v_bfe_u32 v6, v18, 16, 1
	v_bfe_u32 v14, v19, 16, 1
	v_pk_mul_f32 v[38:39], v[38:39], s[4:5] op_sel_hi:[1,0]
	v_bfe_u32 v51, v23, 16, 1
	v_bfe_u32 v52, v22, 16, 1
	v_lshrrev_b32_e32 v26, 16, v26
	v_and_or_b32 v43, v15, s51, v3
	v_bfe_u32 v2, v34, 16, 1
	v_bfe_u32 v3, v35, 16, 1
	v_add3_u32 v14, v19, v14, s50
	v_add3_u32 v6, v18, v6, s50
	v_bfe_u32 v49, v39, 16, 1
	v_bfe_u32 v50, v38, 16, 1
	v_add3_u32 v22, v22, v52, s50
	v_add3_u32 v23, v23, v51, s50
	v_and_or_b32 v44, v30, s51, v26
	v_add3_u32 v3, v35, v3, s50
	v_add3_u32 v2, v34, v2, s50
	v_lshrrev_b32_e32 v6, 16, v6
	v_lshrrev_b32_e32 v14, 16, v14
	v_add3_u32 v31, v38, v50, s50
	v_add3_u32 v38, v39, v49, s50
	global_store_dwordx4 v[8:9], v[42:45], off
	v_lshrrev_b32_e32 v2, 16, v2
	v_lshrrev_b32_e32 v3, 16, v3
	v_and_or_b32 v43, v23, s51, v14
	v_and_or_b32 v42, v22, s51, v6
	v_mov_b32_e32 v22, v32
	v_mov_b32_e32 v23, v40
	v_and_or_b32 v45, v38, s51, v3
	v_and_or_b32 v44, v31, s51, v2
	v_mov_b32_e32 v2, v4
	v_mov_b32_e32 v3, v20
	v_mov_b32_e32 v14, v16
	v_mov_b32_e32 v15, v24
	v_pk_mul_f32 v[22:23], v[22:23], s[4:5] op_sel_hi:[1,0]
	v_pk_mul_f32 v[2:3], v[2:3], s[4:5] op_sel_hi:[1,0]
	v_pk_mul_f32 v[14:15], v[14:15], s[4:5] op_sel_hi:[1,0]
	v_mov_b32_e32 v18, v28
	v_mov_b32_e32 v19, v36
	v_bfe_u32 v4, v23, 16, 1
	v_bfe_u32 v6, v22, 16, 1
	v_pk_mul_f32 v[18:19], v[18:19], s[4:5] op_sel_hi:[1,0]
	v_bfe_u32 v16, v15, 16, 1
	v_bfe_u32 v20, v14, 16, 1
	v_add3_u32 v6, v22, v6, s50
	v_add3_u32 v4, v23, v4, s50
	v_bfe_u32 v22, v2, 16, 1
	v_bfe_u32 v23, v3, 16, 1
	v_add3_u32 v14, v14, v20, s50
	v_add3_u32 v15, v15, v16, s50
	v_bfe_u32 v16, v18, 16, 1
	v_bfe_u32 v20, v19, 16, 1
	v_add3_u32 v3, v3, v23, s50
	v_add3_u32 v2, v2, v22, s50
	v_add3_u32 v19, v19, v20, s50
	v_add3_u32 v16, v18, v16, s50
	v_lshrrev_b32_e32 v2, 16, v2
	v_lshrrev_b32_e32 v3, 16, v3
	v_mov_b32_e32 v24, v17
	global_store_dwordx4 v[8:9], v[42:45], off offset:512
; #define GAS __attribute__((address_space(1)))
; __device__ __forceinline__ unsigned pk2(float lo, float hi) { return f2bf(lo) | (f2bf(hi) << 16); }
; #define NTLD(P) (NT_STREAMS ? __builtin_nontemporal_load(P) : *(P))
;     ...
;     const int nblk = N / 32, kb = item / nblk, nb = item % nblk, a = lane & 7, q = lane >> 3, k0 = 64 * kb + 8 * q, n0 = 32 * nb + 4 * a;
;     const GAS f32x4* src = (const GAS f32x4*)(W + (size_t)k0 * N + n0);
;     f32x4 r[8];
; #pragma unroll
;     for (int i = 0; i < 8; ++i) r[i] = NTLD(src + (size_t)i * (N / 4));
; #pragma unroll
;     for (int j = 0; j < 4; ++j) { v4u o; o.x = pk2(r[0][j] * scale, r[1][j] * scale); o.y = pk2(r[2][j] * scale, r[3][j] * scale); o.z = pk2(r[4][j] * scale, r[5][j] * scale); o.w = pk2(r[6][j] * scale, r[7][j] * scale);
;         if (NT_STREAMS) __builtin_nontemporal_store(o, (GAS v4u*)(WT + (size_t)maprow(mode, n0 + j) * K + k0)); else *(GAS v4u*)(WT + (size_t)maprow(mode, n0 + j) * K + k0) = o; }
;     ...
;     for (int it = it0 + gw; it < it1; it += NGW) {
;         const int e = it / 384, r = it % 384; const size_t eo = (size_t)(layer * 64 + e) * 1024 * 256;
;         if (r < 128) p0_transpose_item(inp(F, I_WGATE) + eo, 1024, 256, UP + (size_t)e * 512 * 1024, 3, scr, r, F.lane);
;         else if (r < 256) p0_transpose_item(inp(F, I_WUP) + eo, 1024, 256, UP + (size_t)e * 512 * 1024, 4, scr, r - 128, F.lane);
;         else p0_transpose_item(inp(F, I_WDOWN) + eo, 256, 1024, DN + (size_t)e * 1024 * 256, 5, scr, r - 256, F.lane, 16.f);
	v_lshrrev_b32_e32 v16, 16, v16
	v_lshrrev_b32_e32 v18, 16, v19
	v_and_or_b32 v43, v15, s51, v3
	v_and_or_b32 v42, v14, s51, v2
	v_pk_mul_f32 v[2:3], v[24:25], s[4:5] op_sel_hi:[1,0]
	v_and_or_b32 v45, v4, s51, v18
	v_and_or_b32 v44, v6, s51, v16
	v_and_b32_sdwa v4, v3, v11 dst_sel:DWORD dst_unused:UNUSED_PAD src0_sel:WORD_1 src1_sel:DWORD
	v_and_b32_sdwa v6, v2, v11 dst_sel:DWORD dst_unused:UNUSED_PAD src0_sel:WORD_1 src1_sel:DWORD
	v_add3_u32 v3, v3, v4, s50
	v_add3_u32 v2, v2, v6, s50
	v_mov_b32_e32 v20, v5
	v_and_b32_e32 v4, 0xffff0000, v3
	v_and_b32_e32 v6, 0xffff0000, v2
	v_pk_mul_f32 v[2:3], v[20:21], s[4:5] op_sel_hi:[1,0]
	v_mov_b32_e32 v28, v33
	v_and_b32_sdwa v5, v3, v11 dst_sel:DWORD dst_unused:UNUSED_PAD src0_sel:WORD_1 src1_sel:DWORD
	v_and_b32_sdwa v14, v2, v11 dst_sel:DWORD dst_unused:UNUSED_PAD src0_sel:WORD_1 src1_sel:DWORD
	v_add3_u32 v3, v3, v5, s50
	v_add3_u32 v2, v2, v14, s50
	v_or_b32_sdwa v3, v4, v3 dst_sel:DWORD dst_unused:UNUSED_PAD src0_sel:DWORD src1_sel:WORD_1
	v_pk_mul_f32 v[4:5], v[28:29], s[4:5] op_sel_hi:[1,0]
	v_or_b32_sdwa v2, v6, v2 dst_sel:DWORD dst_unused:UNUSED_PAD src0_sel:DWORD src1_sel:WORD_1
	v_and_b32_sdwa v6, v5, v11 dst_sel:DWORD dst_unused:UNUSED_PAD src0_sel:WORD_1 src1_sel:DWORD
	v_and_b32_sdwa v14, v4, v11 dst_sel:DWORD dst_unused:UNUSED_PAD src0_sel:WORD_1 src1_sel:DWORD
	v_add3_u32 v5, v5, v6, s50
	v_mov_b32_e32 v36, v41
	v_add3_u32 v4, v4, v14, s50
	v_lshrrev_b32_e32 v5, 16, v5
	v_pk_mul_f32 v[14:15], v[36:37], s[4:5] op_sel_hi:[1,0]
	v_and_or_b32 v4, v4, s51, v5
	v_and_b32_sdwa v5, v15, v11 dst_sel:DWORD dst_unused:UNUSED_PAD src0_sel:WORD_1 src1_sel:DWORD
	v_and_b32_sdwa v6, v14, v11 dst_sel:DWORD dst_unused:UNUSED_PAD src0_sel:WORD_1 src1_sel:DWORD
	v_add3_u32 v5, v15, v5, s50
	v_add3_u32 v6, v14, v6, s50
	v_lshrrev_b32_e32 v5, 16, v5
	global_store_dwordx4 v[8:9], v[42:45], off offset:1024
	v_and_or_b32 v5, v6, s51, v5
	v_lshl_add_u64 v[8:9], v[8:9], 0, s[10:11]
.Lcv0_10:
	s_andn2_b64 vcc, exec, s[16:17]
	s_cbranch_vccnz .Lcv0_12
	v_mov_b32_e32 v2, s52
	ds_read_b64 v[2:3], v2
	s_lshl_b64 s[16:17], s[14:15], 2
	s_waitcnt lgkmcnt(0)
	v_readfirstlane_b32 s30, v2
	v_readfirstlane_b32 s31, v3
	s_add_u32 s16, s30, s16
	s_addc_u32 s17, s31, s17
	s_lshl_b64 s[56:57], s[12:13], 20
	s_add_u32 s56, s9, s56
	s_addc_u32 s57, s18, s57
	s_lshl_b32 s30, s12, 10
	s_sub_i32 s30, s41, s30
	s_and_b32 s30, s30, 0x7c0
	v_bitop3_b32 v42, s30, v12, v1 bitop3:0x36
	s_and_b32 s30, s23, 0xe0
	v_or_b32_e32 v43, s30, v10
	v_lshlrev_b32_e32 v6, 10, v42
	v_lshl_add_u64 v[2:3], s[16:17], 0, v[6:7]
	v_lshlrev_b32_e32 v6, 2, v43
	v_lshl_add_u64 v[8:9], v[2:3], 0, v[6:7]
	global_load_dwordx4 v[2:5], v[8:9], off nt
	global_load_dwordx4 v[14:17], v[8:9], off offset:1024 nt
	global_load_dwordx4 v[18:21], v[8:9], off offset:2048 nt
	global_load_dwordx4 v[22:25], v[8:9], off offset:3072 nt
	v_add_co_u32_e32 v8, vcc, s46, v8
	s_and_b32 s16, s21, 0x100
	s_nop 0
	v_addc_co_u32_e32 v9, vcc, 0, v9, vcc
	global_load_dwordx4 v[26:29], v[8:9], off nt
	global_load_dwordx4 v[30:33], v[8:9], off offset:1024 nt
	global_load_dwordx4 v[34:37], v[8:9], off offset:2048 nt
	global_load_dwordx4 v[38:41], v[8:9], off offset:3072 nt
	v_or_b32_e32 v6, s16, v43
	v_lshlrev_b32_e32 v56, 11, v6
	v_lshlrev_b32_e32 v6, 1, v42
	v_lshl_add_u64 v[8:9], s[56:57], 0, v[6:7]
	v_or_b32_e32 v6, 0x40000, v56
	v_lshl_add_u64 v[52:53], v[8:9], 0, v[6:7]
	v_or_b32_e32 v6, 0x40800, v56
	v_lshl_add_u64 v[54:55], v[8:9], 0, v[6:7]
	s_waitcnt vmcnt(7)
	v_bfe_u32 v6, v2, 16, 1
	s_waitcnt vmcnt(6)
	v_bfe_u32 v42, v14, 16, 1
	s_waitcnt vmcnt(5)
	v_bfe_u32 v43, v18, 16, 1
	s_waitcnt vmcnt(4)
	v_bfe_u32 v44, v22, 16, 1
	v_bfe_u32 v45, v3, 16, 1
	v_add3_u32 v2, v2, v6, s50
	v_add3_u32 v6, v14, v42, s50
	v_add3_u32 v14, v18, v43, s50
	v_add3_u32 v18, v22, v44, s50
	s_waitcnt vmcnt(3)
	v_bfe_u32 v22, v26, 16, 1
	v_bfe_u32 v46, v15, 16, 1
	s_waitcnt vmcnt(2)
	v_bfe_u32 v42, v30, 16, 1
	v_add3_u32 v3, v3, v45, s50
	v_bfe_u32 v45, v27, 16, 1
	v_lshrrev_b32_e32 v2, 16, v2
	v_add3_u32 v22, v26, v22, s50
	v_bfe_u32 v47, v19, 16, 1
	v_bfe_u32 v48, v23, 16, 1
	s_waitcnt vmcnt(1)
	v_bfe_u32 v43, v34, 16, 1
	s_waitcnt vmcnt(0)
	v_bfe_u32 v44, v38, 16, 1
	v_add3_u32 v15, v15, v46, s50
	v_bfe_u32 v46, v31, 16, 1
	v_add3_u32 v26, v30, v42, s50
	v_lshrrev_b32_e32 v3, 16, v3
	v_add3_u32 v27, v27, v45, s50
	v_and_or_b32 v42, v6, s51, v2
	v_lshrrev_b32_e32 v2, 16, v22
	v_add3_u32 v19, v19, v47, s50
	v_add3_u32 v23, v23, v48, s50
	v_bfe_u32 v47, v35, 16, 1
	v_bfe_u32 v48, v39, 16, 1
	v_add3_u32 v30, v34, v43, s50
	v_add3_u32 v34, v38, v44, s50
	v_add3_u32 v31, v31, v46, s50
	v_and_or_b32 v46, v15, s51, v3
	v_lshrrev_b32_e32 v3, 16, v27
	v_and_or_b32 v44, v26, s51, v2
	v_bfe_u32 v2, v28, 16, 1
	v_lshrrev_b32_e32 v14, 16, v14
	v_add3_u32 v35, v35, v47, s50
	v_add3_u32 v38, v39, v48, s50
	v_lshrrev_b32_e32 v6, 16, v30
	v_and_or_b32 v48, v31, s51, v3
	v_add3_u32 v2, v28, v2, s50
	v_bfe_u32 v3, v32, 16, 1
	v_bfe_u32 v49, v4, 16, 1
	v_lshrrev_b32_e32 v19, 16, v19
	v_and_or_b32 v43, v18, s51, v14
	v_lshrrev_b32_e32 v14, 16, v35
	v_and_or_b32 v45, v34, s51, v6
	v_lshrrev_b32_e32 v2, 16, v2
	v_add3_u32 v3, v32, v3, s50
	v_bfe_u32 v51, v20, 16, 1
	v_add3_u32 v4, v4, v49, s50
	v_and_or_b32 v47, v23, s51, v19
	v_and_or_b32 v49, v38, s51, v14
	global_store_dwordx4 v[52:53], v[42:45], off
	global_store_dwordx4 v[54:55], v[46:49], off
	v_and_or_b32 v52, v3, s51, v2
	v_bfe_u32 v2, v36, 16, 1
	v_bfe_u32 v50, v16, 16, 1
	v_bfe_u32 v57, v24, 16, 1
	v_add3_u32 v20, v20, v51, s50
	v_add3_u32 v2, v36, v2, s50
	v_bfe_u32 v3, v40, 16, 1
	v_add3_u32 v16, v16, v50, s50
	v_add3_u32 v24, v24, v57, s50
	v_lshrrev_b32_e32 v4, 16, v4
	v_lshrrev_b32_e32 v20, 16, v20
	v_lshrrev_b32_e32 v2, 16, v2
	v_add3_u32 v3, v40, v3, s50
	v_or_b32_e32 v6, 0x41000, v56
	v_and_or_b32 v50, v16, s51, v4
	v_and_or_b32 v51, v24, s51, v20
	v_and_or_b32 v53, v3, s51, v2
	v_lshl_add_u64 v[2:3], v[8:9], 0, v[6:7]
	global_store_dwordx4 v[2:3], v[50:53], off
	v_bfe_u32 v3, v5, 16, 1
	v_bfe_u32 v2, v17, 16, 1
	v_add3_u32 v3, v5, v3, s50
	v_add3_u32 v2, v17, v2, s50
	v_lshrrev_b32_e32 v3, 16, v3
	v_bfe_u32 v4, v21, 16, 1
	v_and_or_b32 v2, v2, s51, v3
	v_bfe_u32 v3, v25, 16, 1
	v_add3_u32 v4, v21, v4, s50
	v_add3_u32 v3, v25, v3, s50
	v_lshrrev_b32_e32 v4, 16, v4
	v_bfe_u32 v5, v29, 16, 1
	v_and_or_b32 v3, v3, s51, v4
	v_bfe_u32 v4, v33, 16, 1
	v_add3_u32 v5, v29, v5, s50
	v_add3_u32 v4, v33, v4, s50
	v_lshrrev_b32_e32 v5, 16, v5
	v_bfe_u32 v6, v37, 16, 1
	v_and_or_b32 v4, v4, s51, v5
	v_bfe_u32 v5, v41, 16, 1
	v_add3_u32 v6, v37, v6, s50
	v_add3_u32 v5, v41, v5, s50
	v_lshrrev_b32_e32 v6, 16, v6
	v_and_or_b32 v5, v5, s51, v6
	v_or_b32_e32 v6, 0x41800, v56
	v_lshl_add_u64 v[8:9], v[8:9], 0, v[6:7]

; #define GAS __attribute__((address_space(1)))
; __device__ __forceinline__ unsigned pk2(float lo, float hi) { return f2bf(lo) | (f2bf(hi) << 16); }
; #define NTLD(P) (NT_STREAMS ? __builtin_nontemporal_load(P) : *(P))
;     ...
;     const int nblk = N / 32, kb = item / nblk, nb = item % nblk, a = lane & 7, q = lane >> 3, k0 = 64 * kb + 8 * q, n0 = 32 * nb + 4 * a;
;     const GAS f32x4* src = (const GAS f32x4*)(W + (size_t)k0 * N + n0);
;     f32x4 r[8];
; #pragma unroll
;     for (int i = 0; i < 8; ++i) r[i] = NTLD(src + (size_t)i * (N / 4));
; #pragma unroll
;     for (int j = 0; j < 4; ++j) { v4u o; o.x = pk2(r[0][j] * scale, r[1][j] * scale); o.y = pk2(r[2][j] * scale, r[3][j] * scale); o.z = pk2(r[4][j] * scale, r[5][j] * scale); o.w = pk2(r[6][j] * scale, r[7][j] * scale);
;         if (NT_STREAMS) __builtin_nontemporal_store(o, (GAS v4u*)(WT + (size_t)maprow(mode, n0 + j) * K + k0)); else *(GAS v4u*)(WT + (size_t)maprow(mode, n0 + j) * K + k0) = o; }
;     ...
;     for (int it = it0 + gw; it < it1; it += NGW) {
;         const int e = it / 384, r = it % 384; const size_t eo = (size_t)(layer * 64 + e) * 1024 * 256;
;         if (r < 128) p0_transpose_item(inp(F, I_WGATE) + eo, 1024, 256, UP + (size_t)e * 512 * 1024, 3, scr, r, F.lane);
;         else if (r < 256) p0_transpose_item(inp(F, I_WUP) + eo, 1024, 256, UP + (size_t)e * 512 * 1024, 4, scr, r - 128, F.lane);
.Lcv0_13:
	s_andn2_b64 vcc, exec, s[16:17]
	s_cbranch_vccnz .Lcv0_06
	v_mov_b32_e32 v2, s53
	ds_read_b64 v[2:3], v2
	s_lshl_b64 s[14:15], s[14:15], 2
	s_waitcnt lgkmcnt(0)
	v_readfirstlane_b32 s16, v2
	v_readfirstlane_b32 s17, v3
	s_add_u32 s14, s16, s14
	s_addc_u32 s15, s17, s15
	s_lshl_b64 s[12:13], s[12:13], 20
	s_add_u32 s12, s9, s12
	s_addc_u32 s13, s18, s13
	s_bfe_u32 s16, s54, 0x3001c
	s_add_i32 s16, s54, s16
	s_sext_i32_i16 s17, s16
	s_and_b32 s16, s16, 0xfff8
	s_lshl_b32 s17, s17, 3
	s_sub_i32 s16, s54, s16
	s_andn2_b32 s17, s17, 63
	s_sext_i32_i16 s16, s16
	v_or_b32_e32 v8, s17, v1
	s_lshl_b32 s17, s16, 5
	v_ashrrev_i32_e32 v9, 31, v8
	v_or_b32_e32 v2, s17, v10
	v_lshlrev_b64 v[4:5], 10, v[8:9]
	v_lshl_add_u64 v[4:5], s[14:15], 0, v[4:5]
	v_ashrrev_i32_e32 v3, 31, v2
	v_lshl_add_u64 v[26:27], v[2:3], 2, v[4:5]
	global_load_dwordx4 v[2:5], v[26:27], off nt
	global_load_dwordx4 v[14:17], v[26:27], off offset:1024 nt
	global_load_dwordx4 v[18:21], v[26:27], off offset:2048 nt
	global_load_dwordx4 v[22:25], v[26:27], off offset:3072 nt
	v_add_co_u32_e32 v38, vcc, s46, v26
	s_lshl_b32 s14, s16, 6
	s_nop 0
	v_addc_co_u32_e32 v39, vcc, 0, v27, vcc
	global_load_dwordx4 v[26:29], v[38:39], off nt
	global_load_dwordx4 v[30:33], v[38:39], off offset:1024 nt
	global_load_dwordx4 v[34:37], v[38:39], off offset:2048 nt
	s_nop 0
	global_load_dwordx4 v[38:41], v[38:39], off offset:3072 nt
	s_and_b32 s14, s14, 0xffffff00
	v_bitop3_b32 v6, s17, v13, v10 bitop3:0xc8
	v_or_b32_e32 v54, s14, v6
	v_or_b32_e32 v42, 1, v54
	v_ashrrev_i32_e32 v55, 31, v54
	v_ashrrev_i32_e32 v43, 31, v42
	v_lshl_add_u64 v[8:9], v[8:9], 1, s[12:13]
	v_lshlrev_b64 v[44:45], 11, v[54:55]
	v_lshlrev_b64 v[42:43], 11, v[42:43]
	v_lshl_add_u64 v[52:53], v[8:9], 0, v[44:45]
	v_lshl_add_u64 v[56:57], v[8:9], 0, v[42:43]
	s_waitcnt vmcnt(7)
	v_bfe_u32 v6, v2, 16, 1
	s_waitcnt vmcnt(6)
	v_bfe_u32 v42, v14, 16, 1
	s_waitcnt vmcnt(5)
	v_bfe_u32 v43, v18, 16, 1
	s_waitcnt vmcnt(4)
	v_bfe_u32 v44, v22, 16, 1
	v_bfe_u32 v45, v3, 16, 1
	v_add3_u32 v2, v2, v6, s50
	v_add3_u32 v6, v14, v42, s50
	v_add3_u32 v14, v18, v43, s50
	v_add3_u32 v18, v22, v44, s50
	s_waitcnt vmcnt(3)
	v_bfe_u32 v22, v26, 16, 1
	v_bfe_u32 v46, v15, 16, 1
	s_waitcnt vmcnt(2)
	v_bfe_u32 v42, v30, 16, 1
	v_add3_u32 v3, v3, v45, s50
	v_bfe_u32 v45, v27, 16, 1
	v_lshrrev_b32_e32 v2, 16, v2
	v_add3_u32 v22, v26, v22, s50
	v_bfe_u32 v48, v23, 16, 1
	s_waitcnt vmcnt(1)
	v_bfe_u32 v43, v34, 16, 1
	s_waitcnt vmcnt(0)
	v_bfe_u32 v44, v38, 16, 1
	v_add3_u32 v15, v15, v46, s50
	v_bfe_u32 v46, v31, 16, 1
	v_add3_u32 v26, v30, v42, s50
	v_lshrrev_b32_e32 v3, 16, v3
	v_add3_u32 v27, v27, v45, s50
	v_and_or_b32 v42, v6, s51, v2
	v_lshrrev_b32_e32 v2, 16, v22
	v_add3_u32 v23, v23, v48, s50
	v_bfe_u32 v48, v39, 16, 1
	v_add3_u32 v30, v34, v43, s50
	v_add3_u32 v34, v38, v44, s50
	v_add3_u32 v31, v31, v46, s50
	v_and_or_b32 v46, v15, s51, v3
	v_lshrrev_b32_e32 v3, 16, v27
	v_and_or_b32 v44, v26, s51, v2
	v_bfe_u32 v2, v20, 16, 1
	v_add3_u32 v38, v39, v48, s50
	v_and_or_b32 v48, v31, s51, v3
	v_add3_u32 v2, v20, v2, s50
	v_bfe_u32 v3, v24, 16, 1
	v_bfe_u32 v47, v19, 16, 1
	v_lshrrev_b32_e32 v2, 16, v2
	v_add3_u32 v3, v24, v3, s50
	v_add3_u32 v19, v19, v47, s50
	v_bfe_u32 v47, v35, 16, 1
	v_and_or_b32 v51, v3, s51, v2
	v_bfe_u32 v2, v28, 16, 1
	v_lshrrev_b32_e32 v14, 16, v14
	v_add3_u32 v35, v35, v47, s50
	v_lshrrev_b32_e32 v6, 16, v30
	v_add3_u32 v2, v28, v2, s50
	v_bfe_u32 v3, v32, 16, 1
	v_bfe_u32 v49, v4, 16, 1
	v_lshrrev_b32_e32 v19, 16, v19
	v_and_or_b32 v43, v18, s51, v14
	v_lshrrev_b32_e32 v14, 16, v35
	v_and_or_b32 v45, v34, s51, v6
	v_lshrrev_b32_e32 v2, 16, v2
	v_add3_u32 v3, v32, v3, s50
	v_add3_u32 v4, v4, v49, s50
	v_and_or_b32 v47, v23, s51, v19
	v_and_or_b32 v49, v38, s51, v14
	global_store_dwordx4 v[52:53], v[42:45], off
	global_store_dwordx4 v[56:57], v[46:49], off
	v_and_or_b32 v52, v3, s51, v2
	v_bfe_u32 v2, v36, 16, 1
	v_add3_u32 v2, v36, v2, s50
	v_bfe_u32 v3, v40, 16, 1
	v_lshrrev_b32_e32 v2, 16, v2
	v_add3_u32 v3, v40, v3, s50
	v_and_or_b32 v53, v3, s51, v2
	v_or_b32_e32 v2, 2, v54
	v_bfe_u32 v50, v16, 16, 1
	v_ashrrev_i32_e32 v3, 31, v2
	v_add3_u32 v16, v16, v50, s50
	v_lshrrev_b32_e32 v4, 16, v4
	v_lshlrev_b64 v[2:3], 11, v[2:3]
	v_and_or_b32 v50, v16, s51, v4
	v_lshl_add_u64 v[2:3], v[8:9], 0, v[2:3]
	global_store_dwordx4 v[2:3], v[50:53], off
	v_bfe_u32 v3, v5, 16, 1
	v_bfe_u32 v2, v17, 16, 1
	v_add3_u32 v3, v5, v3, s50
	v_add3_u32 v2, v17, v2, s50
	v_lshrrev_b32_e32 v3, 16, v3
	v_bfe_u32 v4, v21, 16, 1
	v_and_or_b32 v2, v2, s51, v3
	v_bfe_u32 v3, v25, 16, 1
	v_add3_u32 v4, v21, v4, s50
	v_add3_u32 v3, v25, v3, s50
	v_lshrrev_b32_e32 v4, 16, v4
	v_bfe_u32 v5, v29, 16, 1
	v_and_or_b32 v3, v3, s51, v4
	v_bfe_u32 v4, v33, 16, 1
	v_add3_u32 v5, v29, v5, s50
	v_or_b32_e32 v14, 3, v54
	v_add3_u32 v4, v33, v4, s50
	v_lshrrev_b32_e32 v5, 16, v5
	v_bfe_u32 v6, v37, 16, 1
	v_and_or_b32 v4, v4, s51, v5
	v_bfe_u32 v5, v41, 16, 1
	v_add3_u32 v6, v37, v6, s50
	v_ashrrev_i32_e32 v15, 31, v14
	v_add3_u32 v5, v41, v5, s50
	v_lshrrev_b32_e32 v6, 16, v6
	v_lshlrev_b64 v[14:15], 11, v[14:15]
	v_and_or_b32 v5, v5, s51, v6
	v_lshl_add_u64 v[8:9], v[8:9], 0, v[14:15]
	s_branch .Lcv0_06

;     ...
;     for (int it = it0 + gw; it < it1; it += NGW) {
;         const int e = it / 384, r = it % 384; const size_t eo = (size_t)(layer * 64 + e) * 1024 * 256;
;         if (r < 128) p0_transpose_item(inp(F, I_WGATE) + eo, 1024, 256, UP + (size_t)e * 512 * 1024, 3, scr, r, F.lane);
;         else if (r < 256) p0_transpose_item(inp(F, I_WUP) + eo, 1024, 256, UP + (size_t)e * 512 * 1024, 4, scr, r - 128, F.lane);
;         else p0_transpose_item(inp(F, I_WDOWN) + eo, 256, 1024, DN + (size_t)e * 1024 * 256, 5, scr, r - 256, F.lane, 16.f);
.Lcv1_07:
	s_mul_hi_i32 s12, s5, 0x2aaaaaab
	s_lshr_b32 s13, s12, 31
	s_ashr_i32 s12, s12, 6
	s_add_i32 s12, s12, s13
	s_mul_i32 s13, s12, 0xfffffe80
	s_add_i32 s54, s5, s13
	s_ashr_i32 s13, s12, 31
	s_lshl_b64 s[14:15], s[12:13], 18
	s_add_u32 s14, s14, 0x1000000
	s_addc_u32 s15, s15, 0
	s_cmpk_gt_i32 s54, 0x7f
	s_mov_b64 s[16:17], -1
	s_cbranch_scc0 .Lcv1_13
	s_cmpk_gt_u32 s54, 0xff
	s_cbranch_scc0 .Lcv1_10
; #define GAS __attribute__((address_space(1)))
; __device__ __forceinline__ unsigned pk2(float lo, float hi) { return f2bf(lo) | (f2bf(hi) << 16); }
; #define NTLD(P) (NT_STREAMS ? __builtin_nontemporal_load(P) : *(P))
;     ...
;     const int nblk = N / 32, kb = item / nblk, nb = item % nblk, a = lane & 7, q = lane >> 3, k0 = 64 * kb + 8 * q, n0 = 32 * nb + 4 * a;
;     const GAS f32x4* src = (const GAS f32x4*)(W + (size_t)k0 * N + n0);
;     f32x4 r[8];
; #pragma unroll
;     for (int i = 0; i < 8; ++i) r[i] = NTLD(src + (size_t)i * (N / 4));
; #pragma unroll
;     for (int j = 0; j < 4; ++j) { v4u o; o.x = pk2(r[0][j] * scale, r[1][j] * scale); o.y = pk2(r[2][j] * scale, r[3][j] * scale); o.z = pk2(r[4][j] * scale, r[5][j] * scale); o.w = pk2(r[6][j] * scale, r[7][j] * scale);
;         if (NT_STREAMS) __builtin_nontemporal_store(o, (GAS v4u*)(WT + (size_t)maprow(mode, n0 + j) * K + k0)); else *(GAS v4u*)(WT + (size_t)maprow(mode, n0 + j) * K + k0) = o; }
;     ...
;         else p0_transpose_item(inp(F, I_WDOWN) + eo, 256, 1024, DN + (size_t)e * 1024 * 256, 5, scr, r - 256, F.lane, 16.f);
	v_mov_b32_e32 v2, s45
	ds_read_b64 v[2:3], v2
	s_lshl_b64 s[16:17], s[14:15], 2
	s_waitcnt lgkmcnt(0)
	v_readfirstlane_b32 s30, v2
	v_readfirstlane_b32 s31, v3
	s_add_u32 s16, s30, s16
	s_addc_u32 s17, s31, s17
	s_lshl_b64 s[56:57], s[12:13], 19
	s_add_u32 s56, s19, s56
	s_addc_u32 s57, s20, s57
	s_lshl_b32 s30, s12, 8
	s_sub_i32 s30, s43, s30
	s_and_b32 s30, s30, 0x1c0
	v_or_b32_e32 v42, s30, v1
	s_and_b32 s30, s23, 0x3e0
	v_or_b32_e32 v4, s30, v10
	v_lshlrev_b32_e32 v6, 12, v42
	v_lshl_add_u64 v[2:3], s[16:17], 0, v[6:7]
	v_lshlrev_b32_e32 v6, 2, v4
	v_lshl_add_u64 v[8:9], v[2:3], 0, v[6:7]
	v_add_co_u32_e32 v18, vcc, s3, v8
	global_load_dwordx4 v[2:5], v[8:9], off nt
	s_nop 0
	v_addc_co_u32_e32 v19, vcc, 0, v9, vcc
	v_add_co_u32_e32 v26, vcc, s47, v8
	global_load_dwordx4 v[14:17], v[18:19], off offset:-4096 nt
	s_nop 0
	global_load_dwordx4 v[18:21], v[18:19], off nt
	v_addc_co_u32_e32 v27, vcc, 0, v9, vcc
	v_add_co_u32_e32 v34, vcc, s48, v8
	global_load_dwordx4 v[22:25], v[26:27], off offset:-4096 nt
	s_nop 0
	global_load_dwordx4 v[26:29], v[26:27], off nt
	v_addc_co_u32_e32 v35, vcc, 0, v9, vcc
	v_add_co_u32_e32 v8, vcc, s49, v8
	global_load_dwordx4 v[30:33], v[34:35], off offset:-4096 nt
	s_nop 0
	global_load_dwordx4 v[34:37], v[34:35], off nt
	v_addc_co_u32_e32 v9, vcc, 0, v9, vcc
	global_load_dwordx4 v[38:41], v[8:9], off nt
	s_lshr_b32 s16, s54, 1
	v_lshlrev_b32_e32 v8, 1, v42
	v_and_b32_e32 v6, 0x3f0, v6
	v_mov_b32_e32 v9, v7
	v_and_or_b32 v6, s16, 12, v6
	v_lshl_add_u64 v[8:9], s[56:57], 0, v[8:9]
	v_lshlrev_b32_e32 v6, 9, v6
	v_lshl_add_u64 v[8:9], v[8:9], 0, v[6:7]
	s_mov_b64 s[16:17], 0
	s_waitcnt vmcnt(7)
	v_mov_b32_e32 v42, v2
	s_waitcnt vmcnt(6)
	v_mov_b32_e32 v44, v14
	s_waitcnt vmcnt(5)
	v_mov_b32_e32 v43, v18
	v_mov_b32_e32 v18, v3
	v_pk_mul_f32 v[2:3], v[42:43], s[4:5] op_sel_hi:[1,0]
	v_pk_mul_f32 v[18:19], v[18:19], s[4:5] op_sel_hi:[1,0]
	s_waitcnt vmcnt(4)
	v_mov_b32_e32 v45, v22
	s_waitcnt vmcnt(3)
	v_mov_b32_e32 v46, v26
	v_mov_b32_e32 v22, v15
	v_pk_mul_f32 v[14:15], v[44:45], s[4:5] op_sel_hi:[1,0]
	v_pk_mul_f32 v[22:23], v[22:23], s[4:5] op_sel_hi:[1,0]
	s_waitcnt vmcnt(2)
	v_mov_b32_e32 v48, v30
	s_waitcnt vmcnt(1)
	v_mov_b32_e32 v47, v34
	v_mov_b32_e32 v34, v27
	v_pk_mul_f32 v[26:27], v[46:47], s[4:5] op_sel_hi:[1,0]
	s_waitcnt vmcnt(0)
	v_mov_b32_e32 v49, v38
	v_mov_b32_e32 v38, v31
	v_pk_mul_f32 v[30:31], v[48:49], s[4:5] op_sel_hi:[1,0]
	v_bfe_u32 v46, v27, 16, 1
	v_bfe_u32 v47, v2, 16, 1
	v_bfe_u32 v6, v31, 16, 1
	v_bfe_u32 v44, v14, 16, 1
	v_bfe_u32 v48, v3, 16, 1
	v_add3_u32 v27, v27, v46, s50
	v_add3_u32 v2, v2, v47, s50
	v_bfe_u32 v42, v30, 16, 1
	v_bfe_u32 v43, v15, 16, 1
	v_bfe_u32 v45, v26, 16, 1
	v_add3_u32 v14, v14, v44, s50
	v_add3_u32 v6, v31, v6, s50
	v_add3_u32 v3, v3, v48, s50
	v_lshrrev_b32_e32 v27, 16, v27
	v_lshrrev_b32_e32 v2, 16, v2
	v_pk_mul_f32 v[34:35], v[34:35], s[4:5] op_sel_hi:[1,0]
	v_add3_u32 v15, v15, v43, s50
	v_add3_u32 v30, v30, v42, s50
	v_add3_u32 v26, v26, v45, s50
	v_lshrrev_b32_e32 v3, 16, v3
	v_and_or_b32 v45, v6, s51, v27
	v_and_or_b32 v42, v14, s51, v2
	v_bfe_u32 v6, v18, 16, 1
	v_bfe_u32 v14, v19, 16, 1
	v_pk_mul_f32 v[38:39], v[38:39], s[4:5] op_sel_hi:[1,0]
	v_bfe_u32 v51, v23, 16, 1
	v_bfe_u32 v52, v22, 16, 1
	v_lshrrev_b32_e32 v26, 16, v26
	v_and_or_b32 v43, v15, s51, v3
	v_bfe_u32 v2, v34, 16, 1
	v_bfe_u32 v3, v35, 16, 1
	v_add3_u32 v14, v19, v14, s50
	v_add3_u32 v6, v18, v6, s50
	v_bfe_u32 v49, v39, 16, 1
	v_bfe_u32 v50, v38, 16, 1
	v_add3_u32 v22, v22, v52, s50
	v_add3_u32 v23, v23, v51, s50
	v_and_or_b32 v44, v30, s51, v26
	v_add3_u32 v3, v35, v3, s50
	v_add3_u32 v2, v34, v2, s50
	v_lshrrev_b32_e32 v6, 16, v6
	v_lshrrev_b32_e32 v14, 16, v14
	v_add3_u32 v31, v38, v50, s50
	v_add3_u32 v38, v39, v49, s50
	global_store_dwordx4 v[8:9], v[42:45], off
	v_lshrrev_b32_e32 v2, 16, v2
	v_lshrrev_b32_e32 v3, 16, v3
	v_and_or_b32 v43, v23, s51, v14
	v_and_or_b32 v42, v22, s51, v6
	v_mov_b32_e32 v22, v32
	v_mov_b32_e32 v23, v40
	v_and_or_b32 v45, v38, s51, v3
	v_and_or_b32 v44, v31, s51, v2
	v_mov_b32_e32 v2, v4
	v_mov_b32_e32 v3, v20
	v_mov_b32_e32 v14, v16
	v_mov_b32_e32 v15, v24
	v_pk_mul_f32 v[22:23], v[22:23], s[4:5] op_sel_hi:[1,0]
	v_pk_mul_f32 v[2:3], v[2:3], s[4:5] op_sel_hi:[1,0]
	v_pk_mul_f32 v[14:15], v[14:15], s[4:5] op_sel_hi:[1,0]
	v_mov_b32_e32 v18, v28
	v_mov_b32_e32 v19, v36
	v_bfe_u32 v4, v23, 16, 1
	v_bfe_u32 v6, v22, 16, 1
	v_pk_mul_f32 v[18:19], v[18:19], s[4:5] op_sel_hi:[1,0]
	v_bfe_u32 v16, v15, 16, 1
	v_bfe_u32 v20, v14, 16, 1
	v_add3_u32 v6, v22, v6, s50
	v_add3_u32 v4, v23, v4, s50
	v_bfe_u32 v22, v2, 16, 1
	v_bfe_u32 v23, v3, 16, 1
	v_add3_u32 v14, v14, v20, s50
	v_add3_u32 v15, v15, v16, s50
	v_bfe_u32 v16, v18, 16, 1
	v_bfe_u32 v20, v19, 16, 1
	v_add3_u32 v3, v3, v23, s50
	v_add3_u32 v2, v2, v22, s50
	v_add3_u32 v19, v19, v20, s50
	v_add3_u32 v16, v18, v16, s50
	v_lshrrev_b32_e32 v2, 16, v2
	v_lshrrev_b32_e32 v3, 16, v3
	v_mov_b32_e32 v24, v17
	global_store_dwordx4 v[8:9], v[42:45], off offset:512
	v_lshrrev_b32_e32 v16, 16, v16
	v_lshrrev_b32_e32 v18, 16, v19
	v_and_or_b32 v43, v15, s51, v3
	v_and_or_b32 v42, v14, s51, v2
	v_pk_mul_f32 v[2:3], v[24:25], s[4:5] op_sel_hi:[1,0]
	v_and_or_b32 v45, v4, s51, v18
	v_and_or_b32 v44, v6, s51, v16
	v_and_b32_sdwa v4, v3, v11 dst_sel:DWORD dst_unused:UNUSED_PAD src0_sel:WORD_1 src1_sel:DWORD
	v_and_b32_sdwa v6, v2, v11 dst_sel:DWORD dst_unused:UNUSED_PAD src0_sel:WORD_1 src1_sel:DWORD
	v_add3_u32 v3, v3, v4, s50
	v_add3_u32 v2, v2, v6, s50
	v_mov_b32_e32 v20, v5
	v_and_b32_e32 v4, 0xffff0000, v3
	v_and_b32_e32 v6, 0xffff0000, v2
	v_pk_mul_f32 v[2:3], v[20:21], s[4:5] op_sel_hi:[1,0]
	v_mov_b32_e32 v28, v33
	v_and_b32_sdwa v5, v3, v11 dst_sel:DWORD dst_unused:UNUSED_PAD src0_sel:WORD_1 src1_sel:DWORD
	v_and_b32_sdwa v14, v2, v11 dst_sel:DWORD dst_unused:UNUSED_PAD src0_sel:WORD_1 src1_sel:DWORD
	v_add3_u32 v3, v3, v5, s50
	v_add3_u32 v2, v2, v14, s50
	v_or_b32_sdwa v3, v4, v3 dst_sel:DWORD dst_unused:UNUSED_PAD src0_sel:DWORD src1_sel:WORD_1
	v_pk_mul_f32 v[4:5], v[28:29], s[4:5] op_sel_hi:[1,0]
	v_or_b32_sdwa v2, v6, v2 dst_sel:DWORD dst_unused:UNUSED_PAD src0_sel:DWORD src1_sel:WORD_1
	v_and_b32_sdwa v6, v5, v11 dst_sel:DWORD dst_unused:UNUSED_PAD src0_sel:WORD_1 src1_sel:DWORD
	v_and_b32_sdwa v14, v4, v11 dst_sel:DWORD dst_unused:UNUSED_PAD src0_sel:WORD_1 src1_sel:DWORD
	v_add3_u32 v5, v5, v6, s50
	v_mov_b32_e32 v36, v41
	v_add3_u32 v4, v4, v14, s50
	v_lshrrev_b32_e32 v5, 16, v5
	v_pk_mul_f32 v[14:15], v[36:37], s[4:5] op_sel_hi:[1,0]
	v_and_or_b32 v4, v4, s51, v5
	v_and_b32_sdwa v5, v15, v11 dst_sel:DWORD dst_unused:UNUSED_PAD src0_sel:WORD_1 src1_sel:DWORD
	v_and_b32_sdwa v6, v14, v11 dst_sel:DWORD dst_unused:UNUSED_PAD src0_sel:WORD_1 src1_sel:DWORD
	v_add3_u32 v5, v15, v5, s50
	v_add3_u32 v6, v14, v6, s50
	v_lshrrev_b32_e32 v5, 16, v5
	global_store_dwordx4 v[8:9], v[42:45], off offset:1024
	v_and_or_b32 v5, v6, s51, v5
	v_lshl_add_u64 v[8:9], v[8:9], 0, s[10:11]
